# speedup vs baseline: 1.0343x; 1.0064x over previous
.LBB0_11:
	v_bfe_u32 v3, v0, 5, 1
	v_lshlrev_b32_e32 v4, 8, v0
	v_and_b32_e32 v4, 0x1f00, v4
	v_and_b32_e32 v5, 7, v0
	v_bitop3_b32 v6, v3, v0, 7 bitop3:0x78
	v_lshl_or_b32 v64, v6, 4, v4
	v_bitop3_b32 v6, v3, v5, 2 bitop3:0x36
	v_lshl_or_b32 v65, v6, 4, v4
	v_bitop3_b32 v6, v3, v5, 4 bitop3:0x36
	v_bitop3_b32 v5, v3, v5, 6 bitop3:0x36
	v_lshl_or_b32 v66, v6, 4, v4
	v_lshl_or_b32 v67, v5, 4, v4
	v_and_b32_e32 v4, 3, v0
	v_lshlrev_b32_e32 v6, 4, v0
	v_lshlrev_b32_e32 v5, 3, v4
	v_and_b32_e32 v6, 0xc0, v6
	v_lshlrev_b32_e32 v8, 1, v0
	v_lshlrev_b32_e32 v9, 8, v3
	v_bfe_u32 v7, v0, 4, 2
	v_and_b32_e32 v8, 32, v8
	v_or3_b32 v5, v5, v9, v6
	s_mov_b32 s0, 0x8000
	v_or3_b32 v184, v5, v8, s0
	v_lshlrev_b32_e32 v5, 8, v7
	v_xor_b32_e32 v6, v7, v1
	s_cmp_lg_u32 0, -1
	v_lshl_or_b32 v222, v6, 4, v5
	v_bitop3_b32 v1, v7, v1, 4 bitop3:0x36
	s_mov_b32 m0, s29
	s_nop 0
	buffer_load_dwordx4 v222, s[12:15], s61 offen lds
	s_cselect_b32 s17, 0, 0
	v_lshl_or_b32 v223, v1, 4, v5
	s_add_i32 s20, s29, 0x400
	s_add_i32 s0, s61, 0x400
	s_mov_b32 m0, s20
	s_nop 0
	buffer_load_dwordx4 v223, s[12:15], s0 offen lds
	v_lshlrev_b32_e32 v0, 6, v0
	s_add_i32 s21, s29, 0x800
	s_add_i32 s0, s61, 0x800
	s_mov_b32 m0, s21
	s_nop 0
	buffer_load_dwordx4 v222, s[12:15], s0 offen lds
	v_and_b32_e32 v0, 0x700, v0
	v_lshlrev_b32_e32 v1, 6, v3
	v_lshlrev_b32_e32 v3, 4, v4
	s_add_i32 s22, s29, 0xc00
	s_add_i32 s1, s61, 0xc00
	s_mov_b32 m0, s22
	s_nop 0
	buffer_load_dwordx4 v223, s[12:15], s1 offen lds
	v_or3_b32 v196, v0, v1, v3
	s_add_i32 s2, s29, 0x8000
	s_mov_b32 m0, s2
	s_nop 0
	buffer_load_dwordx4 v196, s[4:7], s61 offen lds
	s_add_i32 s1, s2, 0x400
	s_add_i32 s3, s61, 0x80
	s_mov_b32 m0, s1
	s_nop 0
	buffer_load_dwordx4 v196, s[4:7], s3 offen lds
	s_add_i32 s1, s2, 0x800
	s_mov_b32 m0, s1
	s_nop 0
	buffer_load_dwordx4 v196, s[4:7], s0 offen lds
	s_add_i32 s0, s2, 0xc00
	s_add_i32 s1, s61, 0x880
	s_mov_b32 m0, s0
	s_nop 0
	buffer_load_dwordx4 v196, s[4:7], s1 offen lds
	s_add_i32 s3, s29, 0x4000
	s_add_i32 s19, s62, 0x0
	s_mov_b32 m0, s3
	s_nop 0
	buffer_load_dwordx4 v222, s[12:15], s19 offen lds
	v_or_b32_e32 v2, 0x10000, v40
	v_add_u32_e32 v218, s17, v64
	v_add_u32_e32 v219, s17, v65
	v_add_u32_e32 v220, s17, v66
	v_add_u32_e32 v221, s17, v67
	s_add_i32 s10, s29, 0x4400
	s_add_i32 s0, s62, 0x400
	s_mov_b32 m0, s10
	s_nop 0
	buffer_load_dwordx4 v223, s[12:15], s0 offen lds
	s_add_i32 s11, s29, 0x4800
	s_add_i32 s18, s62, 0x800
	s_mov_b32 m0, s11
	s_nop 0
	buffer_load_dwordx4 v222, s[12:15], s18 offen lds
	v_add_u32_e32 v32, v2, v218
	v_add_u32_e32 v33, v2, v219
	v_add_u32_e32 v34, v2, v220
	v_add_u32_e32 v35, v2, v221
	s_add_i32 s16, s29, 0x4c00
	s_add_i32 s0, s62, 0xc00
	s_mov_b32 m0, s16
	s_nop 0
	buffer_load_dwordx4 v223, s[12:15], s0 offen lds
	v_add_u32_e32 v212, s17, v184
	ds_read_b128 v[0:3], v32 offset:0
	ds_read_b128 v[4:7], v33 offset:0
	ds_read_b128 v[8:11], v34 offset:0
	ds_read_b128 v[12:15], v35 offset:0
	ds_read_b128 v[16:19], v32 offset:128
	ds_read_b128 v[20:23], v33 offset:128
	ds_read_b128 v[24:27], v34 offset:128
	ds_read_b128 v[28:31], v35 offset:128
	s_waitcnt lgkmcnt(0)
	v_accvgpr_write_b32 a[128], v0
	v_accvgpr_write_b32 a[129], v1
	v_accvgpr_write_b32 a[130], v2
	v_accvgpr_write_b32 a[131], v3
	v_accvgpr_write_b32 a[132], v4
	v_accvgpr_write_b32 a[133], v5
	v_accvgpr_write_b32 a[134], v6
	v_accvgpr_write_b32 a[135], v7
	v_accvgpr_write_b32 a[136], v8
	v_accvgpr_write_b32 a[137], v9
	v_accvgpr_write_b32 a[138], v10
	v_accvgpr_write_b32 a[139], v11
	v_accvgpr_write_b32 a[140], v12
	v_accvgpr_write_b32 a[141], v13
	v_accvgpr_write_b32 a[142], v14
	v_accvgpr_write_b32 a[143], v15
	v_accvgpr_write_b32 a[144], v16
	v_accvgpr_write_b32 a[145], v17
	v_accvgpr_write_b32 a[146], v18
	v_accvgpr_write_b32 a[147], v19
	v_accvgpr_write_b32 a[148], v20
	v_accvgpr_write_b32 a[149], v21
	v_accvgpr_write_b32 a[150], v22
	v_accvgpr_write_b32 a[151], v23
	v_accvgpr_write_b32 a[152], v24
	v_accvgpr_write_b32 a[153], v25
	v_accvgpr_write_b32 a[154], v26
	v_accvgpr_write_b32 a[155], v27
	v_accvgpr_write_b32 a[156], v28
	v_accvgpr_write_b32 a[157], v29
	v_accvgpr_write_b32 a[158], v30
	v_accvgpr_write_b32 a[159], v31
	ds_read_b128 v[0:3], v32 offset:8192
	ds_read_b128 v[4:7], v33 offset:8192
	ds_read_b128 v[8:11], v34 offset:8192
	ds_read_b128 v[12:15], v35 offset:8192
	ds_read_b128 v[16:19], v32 offset:8320
	ds_read_b128 v[20:23], v33 offset:8320
	ds_read_b128 v[24:27], v34 offset:8320
	ds_read_b128 v[28:31], v35 offset:8320
	s_waitcnt lgkmcnt(0)
	v_accvgpr_write_b32 a[160], v0
	v_accvgpr_write_b32 a[161], v1
	v_accvgpr_write_b32 a[162], v2
	v_accvgpr_write_b32 a[163], v3
	v_accvgpr_write_b32 a[164], v4
	v_accvgpr_write_b32 a[165], v5
	v_accvgpr_write_b32 a[166], v6
	v_accvgpr_write_b32 a[167], v7
	v_accvgpr_write_b32 a[168], v8
	v_accvgpr_write_b32 a[169], v9
	v_accvgpr_write_b32 a[170], v10
	v_accvgpr_write_b32 a[171], v11
	v_accvgpr_write_b32 a[172], v12
	v_accvgpr_write_b32 a[173], v13
	v_accvgpr_write_b32 a[174], v14
	v_accvgpr_write_b32 a[175], v15
	v_accvgpr_write_b32 a[176], v16
	v_accvgpr_write_b32 a[177], v17
	v_accvgpr_write_b32 a[178], v18
	v_accvgpr_write_b32 a[179], v19
	v_accvgpr_write_b32 a[180], v20
	v_accvgpr_write_b32 a[181], v21
	v_accvgpr_write_b32 a[182], v22
	v_accvgpr_write_b32 a[183], v23
	v_accvgpr_write_b32 a[184], v24
	v_accvgpr_write_b32 a[185], v25
	v_accvgpr_write_b32 a[186], v26
	v_accvgpr_write_b32 a[187], v27
	v_accvgpr_write_b32 a[188], v28
	v_accvgpr_write_b32 a[189], v29
	v_accvgpr_write_b32 a[190], v30
	v_accvgpr_write_b32 a[191], v31
	s_waitcnt vmcnt(0) lgkmcnt(0)
	s_barrier
	s_nop 0
	ds_read_b128 a[192:195], v218 offset:0
	s_nop 0
	ds_read_b128 a[196:199], v219 offset:0
	ds_read_b128 a[200:203], v220 offset:0
	ds_read_b128 a[204:207], v221 offset:0
	ds_read_b128 a[208:211], v218 offset:128
	ds_read_b128 a[212:215], v219 offset:128
	ds_read_b128 a[216:219], v220 offset:128
	ds_read_b128 a[220:223], v221 offset:128
	ds_read_b128 a[224:227], v218 offset:8192
	ds_read_b128 a[228:231], v219 offset:8192
	ds_read_b128 a[232:235], v220 offset:8192
	ds_read_b128 a[236:239], v221 offset:8192
	ds_read_b128 a[240:243], v218 offset:8320
	ds_read_b128 a[244:247], v219 offset:8320
	ds_read_b128 a[248:251], v220 offset:8320
	ds_read_b128 a[252:255], v221 offset:8320
	s_waitcnt lgkmcnt(0)
	v_mfma_f32_32x32x16_bf16 v[48:63], a[192:195], a[128:131], 0
	v_mfma_f32_32x32x16_bf16 v[32:47], a[192:195], a[160:163], 0
	v_mfma_f32_32x32x16_bf16 v[0:15], a[224:227], a[128:131], 0
	v_mfma_f32_32x32x16_bf16 v[16:31], a[224:227], a[160:163], 0
	v_mfma_f32_32x32x16_bf16 v[48:63], a[196:199], a[132:135], v[48:63]
	v_mfma_f32_32x32x16_bf16 v[32:47], a[196:199], a[164:167], v[32:47]
	v_mfma_f32_32x32x16_bf16 v[0:15], a[228:231], a[132:135], v[0:15]
	v_mfma_f32_32x32x16_bf16 v[16:31], a[228:231], a[164:167], v[16:31]
	v_mfma_f32_32x32x16_bf16 v[48:63], a[200:203], a[136:139], v[48:63]
	v_mfma_f32_32x32x16_bf16 v[32:47], a[200:203], a[168:171], v[32:47]
	v_mfma_f32_32x32x16_bf16 v[0:15], a[232:235], a[136:139], v[0:15]
	v_mfma_f32_32x32x16_bf16 v[16:31], a[232:235], a[168:171], v[16:31]
	v_mfma_f32_32x32x16_bf16 v[48:63], a[204:207], a[140:143], v[48:63]
	v_mfma_f32_32x32x16_bf16 v[32:47], a[204:207], a[172:175], v[32:47]
	v_mfma_f32_32x32x16_bf16 v[0:15], a[236:239], a[140:143], v[0:15]
	v_mfma_f32_32x32x16_bf16 v[16:31], a[236:239], a[172:175], v[16:31]
	v_mfma_f32_32x32x16_bf16 v[48:63], a[208:211], a[144:147], v[48:63]
	s_mov_b32 s27, s29
	v_mfma_f32_32x32x16_bf16 v[32:47], a[208:211], a[176:179], v[32:47]
	s_add_i32 s0, s63, 0x0
	s_mov_b32 s30, s0
	v_mfma_f32_32x32x16_bf16 v[0:15], a[240:243], a[144:147], v[0:15]
	s_mov_b32 s31, s20
	v_mfma_f32_32x32x16_bf16 v[16:31], a[240:243], a[176:179], v[16:31]
	s_add_i32 s33, s63, 0x400
	v_mfma_f32_32x32x16_bf16 v[48:63], a[212:215], a[148:151], v[48:63]
	s_mov_b32 s34, s21
	v_mfma_f32_32x32x16_bf16 v[32:47], a[212:215], a[180:183], v[32:47]
	s_add_i32 s1, s63, 0x800
	s_mov_b32 s35, s1
	v_mfma_f32_32x32x16_bf16 v[0:15], a[244:247], a[148:151], v[0:15]
	s_mov_b32 s36, s22
	v_mfma_f32_32x32x16_bf16 v[16:31], a[244:247], a[180:183], v[16:31]
	s_add_i32 s37, s63, 0xc00
	v_mfma_f32_32x32x16_bf16 v[48:63], a[216:219], a[152:155], v[48:63]
	s_add_i32 s23, s29, 0xc000
	s_mov_b32 s38, s23
	v_mfma_f32_32x32x16_bf16 v[32:47], a[216:219], a[184:187], v[32:47]
	v_mfma_f32_32x32x16_bf16 v[0:15], a[248:251], a[152:155], v[0:15]
	s_add_i32 s24, s29, 0xc400
	s_mov_b32 s39, s24
	v_mfma_f32_32x32x16_bf16 v[16:31], a[248:251], a[184:187], v[16:31]
	s_add_i32 s40, s62, 0x80
	v_mfma_f32_32x32x16_bf16 v[48:63], a[220:223], a[156:159], v[48:63]
	s_add_i32 s25, s29, 0xc800
	s_mov_b32 s41, s25
	v_mfma_f32_32x32x16_bf16 v[32:47], a[220:223], a[188:191], v[32:47]
	v_mfma_f32_32x32x16_bf16 v[0:15], a[252:255], a[156:159], v[0:15]
	s_add_i32 s26, s29, 0xcc00
	s_mov_b32 s42, s26
	v_mfma_f32_32x32x16_bf16 v[16:31], a[252:255], a[188:191], v[16:31]
	s_add_i32 s43, s62, 0x880
	s_waitcnt vmcnt(0) lgkmcnt(0)
	s_barrier
	s_nop 0
	s_mov_b32 m0, s27
	s_nop 0
	buffer_load_dwordx4 v222, s[12:15], s30 offen lds
	s_mov_b32 m0, s31
	s_nop 0
	buffer_load_dwordx4 v223, s[12:15], s33 offen lds
	s_addk_i32 s17, 0x4000
	v_add_u32_e32 v217, s17, v64
	ds_read_b128 a[192:195], v217 offset:0
	s_mov_b32 m0, s34
	s_nop 0
	buffer_load_dwordx4 v222, s[12:15], s35 offen lds
	v_add_u32_e32 v199, s17, v65
	ds_read_b128 a[196:199], v199 offset:0
	s_mov_b32 m0, s36
	s_nop 0
	buffer_load_dwordx4 v223, s[12:15], s37 offen lds
	v_add_u32_e32 v198, s17, v66
	ds_read_b128 a[200:203], v198 offset:0
	s_mov_b32 m0, s38
	s_nop 0
	buffer_load_dwordx4 v196, s[4:7], s19 offen lds
	v_add_u32_e32 v197, s17, v67
	ds_read_b128 a[204:207], v197 offset:0
	s_mov_b32 m0, s39
	s_nop 0
	buffer_load_dwordx4 v196, s[4:7], s40 offen lds
	ds_read_b128 a[208:211], v217 offset:128
	s_mov_b32 m0, s41
	s_nop 0
	buffer_load_dwordx4 v196, s[4:7], s18 offen lds
	ds_read_b128 a[212:215], v199 offset:128
	s_mov_b32 m0, s42
	s_nop 0
	buffer_load_dwordx4 v196, s[4:7], s43 offen lds
	ds_read_b128 a[216:219], v198 offset:128
	ds_read_b128 a[220:223], v197 offset:128
	v_cvt_pk_bf16_f32 v248, v248, v249
	v_cvt_pk_bf16_f32 v249, v250, v251
	v_cvt_pk_bf16_f32 v250, v252, v253
	v_cvt_pk_bf16_f32 v251, v254, v255
	v_lshrrev_b32_e32 v252, 1, v208
	buffer_store_dwordx4 v[248:251], v252, s[12:15], s56 offen sc1
	v_mbcnt_lo_u32_b32 v253, -1, 0
	v_mbcnt_hi_u32_b32 v253, -1, v253
	v_lshlrev_b32_e32 v253, 4, v253
	v_add_u32_e32 v253, s84, v253
	ds_read_b128 v[248:251], v253
	ds_read_b128 v[252:255], v253 offset:1024
	v_max3_f32 v64, v48, v49, v0
	v_max3_f32 v65, v50, v51, v1
	v_max3_f32 v64, v64, v2, v3
	ds_read_b128 a[224:227], v217 offset:8192
	v_max3_f32 v64, v64, v52, v53
	v_max3_f32 v65, v65, v54, v55
	v_max3_f32 v64, v64, v4, v5
	v_max3_f32 v65, v65, v6, v7
	ds_read_b128 a[228:231], v199 offset:8192
	v_max3_f32 v64, v64, v56, v57
	v_max3_f32 v65, v65, v58, v59
	v_max3_f32 v64, v64, v8, v9
	v_max3_f32 v65, v65, v10, v11
	ds_read_b128 a[232:235], v198 offset:8192
	v_max3_f32 v64, v64, v60, v61
	v_max3_f32 v65, v65, v62, v63
	v_max3_f32 v64, v64, v12, v13
	v_max3_f32 v65, v65, v14, v15
	ds_read_b128 a[236:239], v197 offset:8192
	v_max3_f32 v66, v32, v33, v16
	v_max3_f32 v67, v34, v35, v17
	v_max3_f32 v66, v66, v18, v19
	ds_read_b128 a[240:243], v217 offset:8320
	v_max3_f32 v66, v66, v36, v37
	v_max3_f32 v67, v67, v38, v39
	v_max3_f32 v66, v66, v20, v21
	v_max3_f32 v67, v67, v22, v23
	ds_read_b128 a[244:247], v199 offset:8320
	v_max3_f32 v66, v66, v40, v41
	v_max3_f32 v67, v67, v42, v43
	v_max3_f32 v66, v66, v24, v25
	v_max3_f32 v67, v67, v26, v27
	ds_read_b128 a[248:251], v198 offset:8320
	v_max3_f32 v66, v66, v44, v45
	v_max3_f32 v67, v67, v46, v47
	v_max3_f32 v66, v66, v28, v29
	v_max3_f32 v67, v67, v30, v31
	ds_read_b128 a[252:255], v197 offset:8320
	s_waitcnt lgkmcnt(8)
	v_pk_add_f32 v[200:201], v[248:249], v[200:201]
	v_pk_add_f32 v[202:203], v[250:251], v[202:203]
	v_pk_add_f32 v[204:205], v[252:253], v[204:205]
	v_pk_add_f32 v[206:207], v[254:255], v[206:207]
	v_cvt_pk_bf16_f32 v248, v248, v249
	v_cvt_pk_bf16_f32 v249, v250, v251
	v_cvt_pk_bf16_f32 v250, v252, v253
	v_cvt_pk_bf16_f32 v251, v254, v255
	v_lshrrev_b32_e32 v252, 1, v208
	buffer_store_dwordx4 v[248:251], v252, s[4:7], s56 offen sc1
	s_add_i32 s56, s56, 0x1000
	s_nop 1
	global_load_dwordx4 v[248:251], v208, s[54:55] nt
	global_load_dwordx4 v[252:255], v208, s[54:55] offset:16 nt
	s_add_u32 s54, s54, 0x2000
	s_addc_u32 s55, s55, 0
	s_mov_b32 m0, s84
	s_nop 0
	buffer_load_dwordx4 v208, s[80:83], s86 offen lds
	s_mov_b32 m0, s85
	s_nop 0
	buffer_load_dwordx4 v208, s[80:83], s86 offen offset:16 lds
	s_add_i32 s86, s86, 0x2000
	v_max_f32_e32 v64, v64, v65
	v_mov_b32_e32 v65, v64
	s_nop 1
	v_permlane32_swap_b32_e32 v64, v65
	v_max_f32_e32 v214, v64, v65
	v_max_f32_e32 v64, v66, v67
	v_mov_b32_e32 v65, v64
	s_nop 1
	v_permlane32_swap_b32_e32 v64, v65
	v_max_f32_e32 v213, v64, v65
	v_sub_f32_e32 v64, v0, v214
	v_mbcnt_lo_u32_b32 v0, -1, 0
	v_mbcnt_hi_u32_b32 v0, -1, v0
	v_sub_f32_e32 v65, v1, v214
	v_xor_b32_e32 v1, 0x80000000, v214
	v_cmp_gt_u32_e32 vcc, 32, v0
	v_sub_f32_e32 v128, v2, v214
	v_sub_f32_e32 v129, v3, v214
	v_sub_f32_e32 v130, v4, v214
	v_sub_f32_e32 v131, v5, v214
	v_sub_f32_e32 v132, v6, v214
	v_sub_f32_e32 v133, v7, v214
	v_sub_f32_e32 v134, v8, v214
	v_sub_f32_e32 v135, v9, v214
	v_sub_f32_e32 v136, v10, v214
	v_sub_f32_e32 v137, v11, v214
	v_sub_f32_e32 v138, v12, v214
	v_sub_f32_e32 v139, v13, v214
	v_sub_f32_e32 v140, v14, v214
	v_sub_f32_e32 v141, v15, v214
	v_sub_f32_e32 v142, v16, v213
	v_mov_b32_e32 v211, 1.0
	v_sub_f32_e32 v143, v17, v213
	v_xor_b32_e32 v17, 0x80000000, v213
	v_cndmask_b32_e64 v0, 0, 1.0, vcc
	s_nop 1
	v_mfma_f32_32x32x2_f32 v[0:15], v0, v1, 0
	v_mbcnt_lo_u32_b32 v16, -1, 0
	v_mbcnt_hi_u32_b32 v16, -1, v16
	v_sub_f32_e32 v48, v48, v214
	v_sub_f32_e32 v49, v49, v214
	v_sub_f32_e32 v50, v50, v214
	v_sub_f32_e32 v51, v51, v214
	v_sub_f32_e32 v52, v52, v214
	v_sub_f32_e32 v53, v53, v214
	v_sub_f32_e32 v54, v54, v214
	v_sub_f32_e32 v55, v55, v214
	v_sub_f32_e32 v56, v56, v214
	v_sub_f32_e32 v57, v57, v214
	v_sub_f32_e32 v58, v58, v214
	v_sub_f32_e32 v59, v59, v214
	v_sub_f32_e32 v60, v60, v214
	v_sub_f32_e32 v61, v61, v214
	v_sub_f32_e32 v62, v62, v214
	v_sub_f32_e32 v63, v63, v214
	v_sub_f32_e32 v32, v32, v213
	v_sub_f32_e32 v33, v33, v213
	v_sub_f32_e32 v34, v34, v213
	v_cmp_gt_u32_e32 vcc, 32, v16
	v_sub_f32_e32 v35, v35, v213
	v_sub_f32_e32 v36, v36, v213
	v_sub_f32_e32 v37, v37, v213
	v_sub_f32_e32 v38, v38, v213
	v_sub_f32_e32 v39, v39, v213
	v_sub_f32_e32 v40, v40, v213
	v_sub_f32_e32 v41, v41, v213
	v_sub_f32_e32 v42, v42, v213
	v_sub_f32_e32 v43, v43, v213
	v_sub_f32_e32 v44, v44, v213
	v_sub_f32_e32 v45, v45, v213
	v_sub_f32_e32 v46, v46, v213
	v_sub_f32_e32 v47, v47, v213
	v_sub_f32_e32 v144, v18, v213
	v_sub_f32_e32 v145, v19, v213
	v_sub_f32_e32 v146, v20, v213
	v_sub_f32_e32 v147, v21, v213
	v_sub_f32_e32 v183, v22, v213
	v_sub_f32_e32 v194, v23, v213
	v_cndmask_b32_e64 v16, 0, 1.0, vcc
	v_sub_f32_e32 v195, v24, v213
	v_sub_f32_e32 v215, v25, v213
	v_sub_f32_e32 v216, v26, v213
	v_sub_f32_e32 v224, v27, v213
	v_sub_f32_e32 v225, v28, v213
	v_sub_f32_e32 v226, v29, v213
	v_sub_f32_e32 v229, v30, v213
	v_sub_f32_e32 v230, v31, v213
	v_mfma_f32_32x32x2_f32 v[16:31], v16, v17, 0
	v_exp_f32_e32 v112, v48
	v_exp_f32_e32 v113, v49
	v_exp_f32_e32 v114, v50
	v_exp_f32_e32 v115, v51
	v_mov_b32_e32 v193, 0
	v_add_f32_e32 v48, v193, v112
	v_add_f32_e32 v49, v193, v113
	v_exp_f32_e32 v116, v52
	v_exp_f32_e32 v117, v53
	v_exp_f32_e32 v118, v54
	v_add_f32_e32 v48, v48, v114
	v_add_f32_e32 v49, v49, v115
	v_exp_f32_e32 v119, v55
	v_exp_f32_e32 v120, v56
	v_add_f32_e32 v48, v48, v116
	v_add_f32_e32 v49, v49, v117
	v_add_f32_e32 v48, v48, v118
	v_exp_f32_e32 v121, v57
	v_exp_f32_e32 v122, v58
	v_exp_f32_e32 v123, v59
	v_add_f32_e32 v49, v49, v119
	v_add_f32_e32 v48, v48, v120
	v_exp_f32_e32 v124, v60
	v_exp_f32_e32 v125, v61
	v_add_f32_e32 v49, v49, v121
	v_add_f32_e32 v48, v48, v122
	v_add_f32_e32 v49, v49, v123
	v_exp_f32_e32 v126, v62
	v_exp_f32_e32 v127, v63
	v_exp_f32_e32 v96, v32
	v_add_f32_e32 v32, v48, v124
	v_add_f32_e32 v48, v49, v125
	v_exp_f32_e32 v97, v33
	v_exp_f32_e32 v98, v34
	v_add_f32_e32 v231, v32, v126
	v_add_f32_e32 v232, v48, v127
	v_add_f32_e32 v32, v193, v96
	v_exp_f32_e32 v99, v35
	v_exp_f32_e32 v100, v36
	v_exp_f32_e32 v101, v37
	v_add_f32_e32 v33, v193, v97
	v_add_f32_e32 v32, v32, v98
	v_exp_f32_e32 v102, v38
	v_exp_f32_e32 v103, v39
	v_add_f32_e32 v33, v33, v99
	v_add_f32_e32 v32, v32, v100
	v_add_f32_e32 v33, v33, v101
	v_exp_f32_e32 v104, v40
	v_exp_f32_e32 v105, v41
	v_exp_f32_e32 v106, v42
	v_add_f32_e32 v32, v32, v102
	v_add_f32_e32 v33, v33, v103
	v_exp_f32_e32 v107, v43
	v_exp_f32_e32 v108, v44
	v_add_f32_e32 v32, v32, v104
	v_add_f32_e32 v33, v33, v105
	v_add_f32_e32 v32, v32, v106
	v_exp_f32_e32 v109, v45
	v_exp_f32_e32 v110, v46
	v_exp_f32_e32 v111, v47
	v_add_f32_e32 v33, v33, v107
	v_add_f32_e32 v32, v32, v108
	s_waitcnt lgkmcnt(0)
	v_add_f32_e32 v33, v33, v109
	v_add_f32_e32 v233, v32, v110
	v_add_f32_e32 v234, v33, v111
	v_mfma_f32_32x32x16_bf16 v[80:95], a[192:195], a[128:131], v[0:15]
	ds_read_b64_tr_b16 v[160:161], v212 offset:0
	v_exp_f32_e32 v235, v64
	v_exp_f32_e32 v236, v65
	v_cvt_pk_bf16_f32 v152, v112, v113
	v_mfma_f32_32x32x16_bf16 v[64:79], a[192:195], a[160:163], v[16:31]
	ds_read_b64_tr_b16 v[162:163], v212 offset:0x800
	v_exp_f32_e32 v237, v128
	v_exp_f32_e32 v238, v129
	v_cvt_pk_bf16_f32 v153, v114, v115
	v_exp_f32_e32 v115, v130
	v_mfma_f32_32x32x16_bf16 v[48:63], a[224:227], a[128:131], v[0:15]
	ds_read_b64_tr_b16 v[172:173], v212 offset:0x200
	v_exp_f32_e32 v239, v131
	v_cvt_pk_bf16_f32 v154, v116, v117
	v_mfma_f32_32x32x16_bf16 v[32:47], a[224:227], a[160:163], v[16:31]
	ds_read_b64_tr_b16 v[174:175], v212 offset:0xa00
	ds_read_b64_tr_b16 v[168:169], v212 offset:0x400
	v_exp_f32_e32 v240, v132
	v_exp_f32_e32 v241, v133
	v_cvt_pk_bf16_f32 v155, v118, v119
	v_exp_f32_e32 v185, v134
	v_exp_f32_e32 v186, v135
	v_mfma_f32_32x32x16_bf16 v[80:95], a[196:199], a[132:135], v[80:95]
	ds_read_b64_tr_b16 v[170:171], v212 offset:0xc00
	v_cvt_pk_bf16_f32 v128, v120, v121
	v_exp_f32_e32 v187, v136
	v_exp_f32_e32 v188, v137
	v_mfma_f32_32x32x16_bf16 v[64:79], a[196:199], a[164:167], v[64:79]
	ds_read_b64_tr_b16 v[176:177], v212 offset:0x600
	v_cvt_pk_bf16_f32 v129, v122, v123
	v_exp_f32_e32 v189, v138
	v_exp_f32_e32 v190, v139
	v_mfma_f32_32x32x16_bf16 v[48:63], a[228:231], a[132:135], v[48:63]
	ds_read_b64_tr_b16 v[178:179], v212 offset:0xe00
	v_cvt_pk_bf16_f32 v130, v124, v125
	v_mfma_f32_32x32x16_bf16 v[32:47], a[228:231], a[164:167], v[32:47]
	ds_read_b64_tr_b16 v[164:165], v212 offset:0x1000
	v_exp_f32_e32 v191, v140
	v_exp_f32_e32 v192, v141
	ds_read_b64_tr_b16 v[166:167], v212 offset:0x1800
	v_cvt_pk_bf16_f32 v131, v126, v127
	v_exp_f32_e32 v141, v142
	v_exp_f32_e32 v142, v143
	v_mfma_f32_32x32x16_bf16 v[80:95], a[200:203], a[136:139], v[80:95]
	ds_read_b64_tr_b16 v[156:157], v212 offset:0x1200
	v_cvt_pk_bf16_f32 v180, v96, v97
	v_exp_f32_e32 v143, v144
	v_mfma_f32_32x32x16_bf16 v[64:79], a[200:203], a[168:171], v[64:79]
	ds_read_b64_tr_b16 v[158:159], v212 offset:0x1a00
	v_exp_f32_e32 v242, v145
	v_cvt_pk_bf16_f32 v181, v98, v99
	v_mfma_f32_32x32x16_bf16 v[48:63], a[232:235], a[136:139], v[48:63]
	ds_read_b64_tr_b16 v[148:149], v212 offset:0x1400
	v_exp_f32_e32 v243, v146
	v_exp_f32_e32 v244, v147
	v_cvt_pk_bf16_f32 v182, v100, v101
	v_mfma_f32_32x32x16_bf16 v[32:47], a[232:235], a[168:171], v[32:47]
	ds_read_b64_tr_b16 v[150:151], v212 offset:0x1c00
	ds_read_b64_tr_b16 v[136:137], v212 offset:0x1600
	v_exp_f32_e32 v245, v183
	v_exp_f32_e32 v246, v194
	v_cvt_pk_bf16_f32 v183, v102, v103
	v_exp_f32_e32 v194, v195
	v_exp_f32_e32 v195, v215
	v_mfma_f32_32x32x16_bf16 v[80:95], a[204:207], a[140:143], v[80:95]
	ds_read_b64_tr_b16 v[138:139], v212 offset:0x1e00
	v_cvt_pk_bf16_f32 v144, v104, v105
	v_exp_f32_e32 v215, v216
	v_exp_f32_e32 v224, v224
	v_mfma_f32_32x32x16_bf16 v[64:79], a[204:207], a[172:175], v[64:79]
	ds_read_b64_tr_b16 v[132:133], v212 offset:0x2000
	v_cvt_pk_bf16_f32 v145, v106, v107
	v_exp_f32_e32 v227, v225
	v_exp_f32_e32 v228, v226
	v_mfma_f32_32x32x16_bf16 v[48:63], a[236:239], a[140:143], v[48:63]
	ds_read_b64_tr_b16 v[134:135], v212 offset:0x2800
	v_cvt_pk_bf16_f32 v146, v108, v109
	v_mfma_f32_32x32x16_bf16 v[32:47], a[236:239], a[172:175], v[32:47]
	ds_read_b64_tr_b16 v[124:125], v212 offset:0x2200
	v_exp_f32_e32 v229, v229
	v_exp_f32_e32 v230, v230
	ds_read_b64_tr_b16 v[126:127], v212 offset:0x2a00
	v_cvt_pk_bf16_f32 v147, v110, v111
	s_mov_b32 s27, s3
	v_mfma_f32_32x32x16_bf16 v[80:95], a[208:211], a[144:147], v[80:95]
	ds_read_b64_tr_b16 v[120:121], v212 offset:0x2400
	v_cvt_pk_bf16_f32 v112, v235, v236
	v_add_f32_e32 v96, v231, v235
	v_add_f32_e32 v97, v232, v236
	s_add_i32 s30, s87, 0x0
	v_mfma_f32_32x32x16_bf16 v[64:79], a[208:211], a[176:179], v[64:79]
	ds_read_b64_tr_b16 v[122:123], v212 offset:0x2c00
	v_cvt_pk_bf16_f32 v113, v237, v238
	v_add_f32_e32 v96, v96, v237
	v_add_f32_e32 v97, v97, v238
	s_mov_b32 s31, s10
	v_mfma_f32_32x32x16_bf16 v[48:63], a[240:243], a[144:147], v[48:63]
	ds_read_b64_tr_b16 v[116:117], v212 offset:0x2600
	v_cvt_pk_bf16_f32 v114, v115, v239
	v_add_f32_e32 v96, v96, v115
	v_add_f32_e32 v97, v97, v239
	s_add_i32 s33, s87, 0x400
	v_mfma_f32_32x32x16_bf16 v[32:47], a[240:243], a[176:179], v[32:47]
	ds_read_b64_tr_b16 v[118:119], v212 offset:0x2e00
	ds_read_b64_tr_b16 v[104:105], v212 offset:0x3000
	v_cvt_pk_bf16_f32 v115, v240, v241
	v_add_f32_e32 v96, v96, v240
	v_add_f32_e32 v97, v97, v241
	s_mov_b32 s34, s11
	v_mfma_f32_32x32x16_bf16 v[80:95], a[212:215], a[148:151], v[80:95]
	ds_read_b64_tr_b16 v[106:107], v212 offset:0x3800
	v_add_f32_e32 v96, v96, v185
	v_add_f32_e32 v97, v97, v186
	s_add_i32 s35, s87, 0x800
	v_mfma_f32_32x32x16_bf16 v[64:79], a[212:215], a[180:183], v[64:79]
	ds_read_b64_tr_b16 v[108:109], v212 offset:0x3200
	v_add_f32_e32 v96, v96, v187
	v_add_f32_e32 v97, v97, v188
	s_mov_b32 s36, s16
	v_mfma_f32_32x32x16_bf16 v[48:63], a[244:247], a[148:151], v[48:63]
	ds_read_b64_tr_b16 v[110:111], v212 offset:0x3a00
	v_add_f32_e32 v96, v96, v189
	v_add_f32_e32 v97, v97, v190
	s_add_i32 s37, s87, 0xc00
	v_mfma_f32_32x32x16_bf16 v[32:47], a[244:247], a[180:183], v[32:47]
	ds_read_b64_tr_b16 v[100:101], v212 offset:0x3400
	ds_read_b64_tr_b16 v[102:103], v212 offset:0x3c00
	v_add_f32_e32 v216, v96, v191
	v_add_f32_e32 v225, v97, v192
	s_mov_b32 s38, s2
	v_mfma_f32_32x32x16_bf16 v[80:95], a[216:219], a[152:155], v[80:95]
	ds_read_b64_tr_b16 v[96:97], v212 offset:0x3600
	v_cvt_pk_bf16_f32 v140, v141, v142
	v_add_f32_e32 v226, v233, v141
	v_add_f32_e32 v142, v234, v142
	v_mfma_f32_32x32x16_bf16 v[64:79], a[216:219], a[184:187], v[64:79]
	ds_read_b64_tr_b16 v[98:99], v212 offset:0x3e00
	v_cvt_pk_bf16_f32 v141, v143, v242
	v_add_f32_e32 v143, v226, v143
	v_add_f32_e32 v226, v142, v242
	v_mfma_f32_32x32x16_bf16 v[48:63], a[248:251], a[152:155], v[48:63]
	s_add_i32 s17, s29, 0x8400
	s_mov_b32 s39, s17
	v_cvt_pk_bf16_f32 v142, v243, v244
	v_add_f32_e32 v231, v143, v243
	v_add_f32_e32 v226, v226, v244
	v_mfma_f32_32x32x16_bf16 v[32:47], a[248:251], a[184:187], v[32:47]
	s_add_i32 s40, s63, 0x80
	v_cvt_pk_bf16_f32 v143, v245, v246
	v_add_f32_e32 v231, v231, v245
	v_add_f32_e32 v226, v226, v246
	v_mfma_f32_32x32x16_bf16 v[80:95], a[220:223], a[156:159], v[80:95]
	s_add_i32 s18, s29, 0x8800
	s_mov_b32 s41, s18
	v_add_f32_e32 v231, v231, v194
	v_add_f32_e32 v226, v226, v195
	v_mfma_f32_32x32x16_bf16 v[64:79], a[220:223], a[188:191], v[64:79]
	v_add_f32_e32 v231, v231, v215
	v_add_f32_e32 v226, v226, v224
	v_mfma_f32_32x32x16_bf16 v[48:63], a[252:255], a[156:159], v[48:63]
	s_add_i32 s19, s29, 0x8c00
	s_mov_b32 s42, s19
	v_add_f32_e32 v231, v231, v227
	v_add_f32_e32 v226, v226, v228
	v_mfma_f32_32x32x16_bf16 v[32:47], a[252:255], a[188:191], v[32:47]
	s_add_i32 s43, s63, 0x880
	v_add_f32_e32 v231, v231, v229
	v_add_f32_e32 v226, v226, v230
	v_add_f32_e32 v216, v216, v225
	s_waitcnt vmcnt(0) lgkmcnt(0)
	s_barrier
	s_mov_b32 m0, s27
	v_mfma_f32_32x32x16_bf16 a[0:15], v[160:163], v[152:155], 0
	v_mov_b32_e32 v225, v216
	buffer_load_dwordx4 v222, s[12:15], s30 offen lds
	s_mov_b32 m0, s31
	v_mfma_f32_32x32x16_bf16 a[16:31], v[160:163], v[180:183], 0
	v_permlane32_swap_b32_e32 v216, v225
	v_add_f32_e32 v216, v216, v225
	buffer_load_dwordx4 v223, s[12:15], s33 offen lds
	ds_read_b128 a[192:195], v218 offset:0
	s_mov_b32 m0, s34
	v_mfma_f32_32x32x16_bf16 a[32:47], v[172:175], v[152:155], 0
	v_add_f32_e32 v225, v193, v216
	v_add_f32_e32 v216, v231, v226
	v_mov_b32_e32 v226, v216
	buffer_load_dwordx4 v222, s[12:15], s35 offen lds
	ds_read_b128 a[196:199], v219 offset:0
	s_mov_b32 m0, s36
	v_mfma_f32_32x32x16_bf16 a[48:63], v[172:175], v[180:183], 0
	v_permlane32_swap_b32_e32 v216, v226
	v_add_f32_e32 v216, v216, v226
	buffer_load_dwordx4 v223, s[12:15], s37 offen lds
	ds_read_b128 a[200:203], v220 offset:0
	s_mov_b32 m0, s38
	v_mfma_f32_32x32x16_bf16 a[64:79], v[168:171], v[152:155], 0
	v_add_f32_e32 v226, v193, v216
	buffer_load_dwordx4 v196, s[4:7], s0 offen lds
	ds_read_b128 a[204:207], v221 offset:0
	s_mov_b32 m0, s39
	v_mfma_f32_32x32x16_bf16 a[80:95], v[168:171], v[180:183], 0
	buffer_load_dwordx4 v196, s[4:7], s40 offen lds
	ds_read_b128 a[208:211], v218 offset:128
	s_mov_b32 m0, s41
	v_mfma_f32_32x32x16_bf16 a[96:111], v[176:179], v[152:155], 0
	buffer_load_dwordx4 v196, s[4:7], s1 offen lds
	ds_read_b128 a[212:215], v219 offset:128
	s_mov_b32 m0, s42
	v_mfma_f32_32x32x16_bf16 a[112:127], v[176:179], v[180:183], 0
	buffer_load_dwordx4 v196, s[4:7], s43 offen lds
	ds_read_b128 a[216:219], v220 offset:128
	v_mfma_f32_32x32x16_bf16 a[0:15], v[164:167], v[128:131], a[0:15]
	ds_read_b128 a[220:223], v221 offset:128
	v_cvt_pk_bf16_f32 v248, v248, v249
	v_cvt_pk_bf16_f32 v249, v250, v251
	v_cvt_pk_bf16_f32 v250, v252, v253
	v_cvt_pk_bf16_f32 v251, v254, v255
	v_lshrrev_b32_e32 v252, 1, v208
	buffer_store_dwordx4 v[248:251], v252, s[12:15], s56 offen sc1
	v_mbcnt_lo_u32_b32 v253, -1, 0
	v_mbcnt_hi_u32_b32 v253, -1, v253
	v_lshlrev_b32_e32 v253, 4, v253
	v_add_u32_e32 v253, s84, v253
	ds_read_b128 v[248:251], v253
	ds_read_b128 v[252:255], v253 offset:1024
	v_max3_f32 v152, v80, v81, v48
	v_max3_f32 v153, v82, v83, v49
	v_max3_f32 v152, v152, v50, v51
	v_mfma_f32_32x32x16_bf16 a[16:31], v[164:167], v[144:147], a[16:31]
	ds_read_b128 a[224:227], v218 offset:8192
	v_max3_f32 v152, v152, v84, v85
	v_max3_f32 v153, v153, v86, v87
	v_max3_f32 v152, v152, v52, v53
	v_max3_f32 v153, v153, v54, v55
	v_mfma_f32_32x32x16_bf16 a[32:47], v[156:159], v[128:131], a[32:47]
	ds_read_b128 a[228:231], v219 offset:8192
	v_max3_f32 v152, v152, v88, v89
	v_max3_f32 v153, v153, v90, v91
	v_max3_f32 v152, v152, v56, v57
	v_max3_f32 v153, v153, v58, v59
	v_mfma_f32_32x32x16_bf16 a[48:63], v[156:159], v[144:147], a[48:63]
	ds_read_b128 a[232:235], v220 offset:8192
	v_max3_f32 v152, v152, v92, v93
	v_max3_f32 v153, v153, v94, v95
	v_max3_f32 v152, v152, v60, v61
	v_max3_f32 v153, v153, v62, v63
	v_mfma_f32_32x32x16_bf16 a[64:79], v[148:151], v[128:131], a[64:79]
	ds_read_b128 a[236:239], v221 offset:8192
	v_max3_f32 v154, v64, v65, v32
	v_max3_f32 v155, v66, v67, v33
	v_max3_f32 v154, v154, v34, v35
	v_mfma_f32_32x32x16_bf16 a[80:95], v[148:151], v[144:147], a[80:95]
	ds_read_b128 a[240:243], v218 offset:8320
	v_max3_f32 v148, v154, v68, v69
	v_max3_f32 v149, v155, v70, v71
	v_max3_f32 v148, v148, v36, v37
	v_max3_f32 v149, v149, v38, v39
	v_mfma_f32_32x32x16_bf16 a[96:111], v[136:139], v[128:131], a[96:111]
	ds_read_b128 a[244:247], v219 offset:8320
	v_max3_f32 v128, v148, v72, v73
	v_max3_f32 v129, v149, v74, v75
	v_max3_f32 v128, v128, v40, v41
	v_max3_f32 v129, v129, v42, v43
	v_mfma_f32_32x32x16_bf16 a[112:127], v[136:139], v[144:147], a[112:127]
	ds_read_b128 a[248:251], v220 offset:8320
	v_max3_f32 v128, v128, v76, v77
	v_max3_f32 v129, v129, v78, v79
	v_max3_f32 v128, v128, v44, v45
	v_max3_f32 v130, v129, v46, v47
	v_mfma_f32_32x32x16_bf16 a[0:15], v[132:135], v[112:115], a[0:15]
	ds_read_b128 a[252:255], v221 offset:8320
	s_waitcnt lgkmcnt(8)
	v_pk_add_f32 v[200:201], v[248:249], v[200:201]
	v_pk_add_f32 v[202:203], v[250:251], v[202:203]
	v_pk_add_f32 v[204:205], v[252:253], v[204:205]
	v_pk_add_f32 v[206:207], v[254:255], v[206:207]
	v_cvt_pk_bf16_f32 v248, v248, v249
	v_cvt_pk_bf16_f32 v249, v250, v251
	v_cvt_pk_bf16_f32 v250, v252, v253
	v_cvt_pk_bf16_f32 v251, v254, v255
	v_lshrrev_b32_e32 v252, 1, v208
	buffer_store_dwordx4 v[248:251], v252, s[4:7], s56 offen sc1
	s_add_i32 s56, s56, 0x1000
	s_nop 1
	global_load_dwordx4 v[248:251], v208, s[54:55] nt
	global_load_dwordx4 v[252:255], v208, s[54:55] offset:16 nt
	s_add_u32 s54, s54, 0x2000
	s_addc_u32 s55, s55, 0
	s_mov_b32 m0, s84
	s_nop 0
	buffer_load_dwordx4 v208, s[80:83], s86 offen lds
	s_mov_b32 m0, s85
	s_nop 0
	buffer_load_dwordx4 v208, s[80:83], s86 offen offset:16 lds
	s_add_i32 s86, s86, 0x2000
	v_max_f32_e32 v129, v152, v153
	v_mov_b32_e32 v131, v129
	s_nop 1
	v_permlane32_swap_b32_e32 v129, v131
	v_max_f32_e32 v129, v129, v131
	v_mfma_f32_32x32x16_bf16 a[16:31], v[132:135], v[140:143], a[16:31]
	v_max_f32_e32 v128, v128, v130
	v_mov_b32_e32 v130, v128
	s_nop 1
	v_permlane32_swap_b32_e32 v128, v130
	v_max_f32_e32 v128, v128, v130
	v_max_f32_e32 v130, v129, v129
	v_max_f32_e32 v131, v128, v128
	v_max_f32_e32 v130, v130, v131
	s_mov_b32 s0, 0x41000000
	v_mfma_f32_32x32x16_bf16 a[32:47], v[124:127], v[112:115], a[32:47]
	v_cmp_lt_f32_e32 vcc, s0, v130
	s_cmp_lg_u64 vcc, 0
	s_cselect_b64 s[0:1], -1, 0
	s_cbranch_vccnz .LBB0_41
	v_mov_b32_e32 v216, 1.0

.LBB0_17:
	v_mfma_f32_32x32x16_bf16 v[112:127], a[192:195], a[128:131], v[0:15]
	v_exp_f32_e32 v48, v48
	v_exp_f32_e32 v49, v49
	ds_read_b64_tr_b16 v[172:173], v215 offset:0
	v_cvt_pk_bf16_f32 v164, v128, v129
	v_exp_f32_e32 v50, v50
	v_exp_f32_e32 v51, v51
	v_mfma_f32_32x32x16_bf16 v[96:111], a[192:195], a[160:163], v[16:31]
	ds_read_b64_tr_b16 v[174:175], v215 offset:0x800
	v_cvt_pk_bf16_f32 v165, v130, v131
	v_mfma_f32_32x32x16_bf16 v[80:95], a[224:227], a[128:131], v[0:15]
	ds_read_b64_tr_b16 v[184:185], v215 offset:0x200
	v_exp_f32_e32 v239, v52
	v_exp_f32_e32 v240, v53
	v_cvt_pk_bf16_f32 v166, v132, v133
	v_mfma_f32_32x32x16_bf16 v[64:79], a[224:227], a[160:163], v[16:31]
	ds_read_b64_tr_b16 v[186:187], v215 offset:0xa00
	ds_read_b64_tr_b16 v[180:181], v215 offset:0x400
	v_exp_f32_e32 v241, v54
	v_exp_f32_e32 v242, v55
	v_cvt_pk_bf16_f32 v167, v134, v135
	v_exp_f32_e32 v227, v56
	v_exp_f32_e32 v228, v57
	v_mfma_f32_32x32x16_bf16 v[112:127], a[196:199], a[132:135], v[112:127]
	ds_read_b64_tr_b16 v[182:183], v215 offset:0xc00
	v_cvt_pk_bf16_f32 v128, v136, v137
	v_exp_f32_e32 v229, v58
	v_exp_f32_e32 v230, v59
	v_mfma_f32_32x32x16_bf16 v[96:111], a[196:199], a[164:167], v[96:111]
	ds_read_b64_tr_b16 v[188:189], v215 offset:0x600
	v_cvt_pk_bf16_f32 v129, v138, v139
	v_exp_f32_e32 v231, v60
	v_exp_f32_e32 v232, v61
	v_mfma_f32_32x32x16_bf16 v[80:95], a[228:231], a[132:135], v[80:95]
	ds_read_b64_tr_b16 v[190:191], v215 offset:0xe00
	v_cvt_pk_bf16_f32 v130, v140, v141
	v_mfma_f32_32x32x16_bf16 v[64:79], a[228:231], a[164:167], v[64:79]
	ds_read_b64_tr_b16 v[176:177], v215 offset:0x1000
	v_exp_f32_e32 v233, v62
	v_exp_f32_e32 v234, v63
	ds_read_b64_tr_b16 v[178:179], v215 offset:0x1800
	v_cvt_pk_bf16_f32 v131, v142, v143
	v_exp_f32_e32 v141, v32
	v_exp_f32_e32 v142, v33
	v_mfma_f32_32x32x16_bf16 v[112:127], a[200:203], a[136:139], v[112:127]
	ds_read_b64_tr_b16 v[168:169], v215 offset:0x1200
	v_cvt_pk_bf16_f32 v192, v144, v145
	v_exp_f32_e32 v143, v34
	v_mfma_f32_32x32x16_bf16 v[96:111], a[200:203], a[168:171], v[96:111]
	ds_read_b64_tr_b16 v[170:171], v215 offset:0x1a00
	v_exp_f32_e32 v243, v35
	v_cvt_pk_bf16_f32 v193, v146, v147
	v_mfma_f32_32x32x16_bf16 v[80:95], a[232:235], a[136:139], v[80:95]
	ds_read_b64_tr_b16 v[160:161], v215 offset:0x1400
	v_exp_f32_e32 v244, v36
	v_exp_f32_e32 v245, v37
	v_cvt_pk_bf16_f32 v194, v148, v149
	v_mfma_f32_32x32x16_bf16 v[64:79], a[232:235], a[168:171], v[64:79]
	ds_read_b64_tr_b16 v[162:163], v215 offset:0x1c00
	ds_read_b64_tr_b16 v[136:137], v215 offset:0x1600
	v_exp_f32_e32 v246, v38
	v_exp_f32_e32 v247, v39
	v_cvt_pk_bf16_f32 v195, v150, v151
	v_exp_f32_e32 v148, v40
	v_exp_f32_e32 v149, v41
	v_mfma_f32_32x32x16_bf16 v[112:127], a[204:207], a[140:143], v[112:127]
	ds_read_b64_tr_b16 v[138:139], v215 offset:0x1e00
	v_cvt_pk_bf16_f32 v144, v152, v153
	v_exp_f32_e32 v150, v42
	v_exp_f32_e32 v151, v43
	v_mfma_f32_32x32x16_bf16 v[96:111], a[204:207], a[172:175], v[96:111]
	ds_read_b64_tr_b16 v[132:133], v215 offset:0x2000
	v_cvt_pk_bf16_f32 v145, v154, v155
	v_exp_f32_e32 v152, v44
	v_exp_f32_e32 v153, v45
	v_mfma_f32_32x32x16_bf16 v[80:95], a[236:239], a[140:143], v[80:95]
	ds_read_b64_tr_b16 v[134:135], v215 offset:0x2800
	v_cvt_pk_bf16_f32 v146, v156, v157
	v_mfma_f32_32x32x16_bf16 v[64:79], a[236:239], a[172:175], v[64:79]
	ds_read_b64_tr_b16 v[60:61], v215 offset:0x2200
	v_exp_f32_e32 v154, v46
	v_exp_f32_e32 v155, v47
	ds_read_b64_tr_b16 v[62:63], v215 offset:0x2a00
	v_cvt_pk_bf16_f32 v147, v158, v159
	s_mov_b32 s0, s29
	v_mfma_f32_32x32x16_bf16 v[112:127], a[208:211], a[144:147], v[112:127]
	ds_read_b64_tr_b16 v[56:57], v215 offset:0x2400
	v_cvt_pk_bf16_f32 v52, v48, v49
	v_add_f32_e32 v32, v236, v48
	v_add_f32_e32 v33, v235, v49
	s_add_i32 s57, s58, s59
	s_and_b32 s57, s57, 0x7ffff
	s_mov_b32 s33, s57
	s_mov_b32 s1, s33
	v_mfma_f32_32x32x16_bf16 v[96:111], a[208:211], a[176:179], v[96:111]
	ds_read_b64_tr_b16 v[58:59], v215 offset:0x2c00
	v_cvt_pk_bf16_f32 v53, v50, v51
	v_add_f32_e32 v32, v32, v50
	v_add_f32_e32 v33, v33, v51
	s_mov_b32 s35, s20
	v_mfma_f32_32x32x16_bf16 v[80:95], a[240:243], a[144:147], v[80:95]
	ds_read_b64_tr_b16 v[48:49], v215 offset:0x2600
	v_cvt_pk_bf16_f32 v54, v239, v240
	v_add_f32_e32 v32, v32, v239
	v_add_f32_e32 v33, v33, v240
	s_add_i32 s36, s57, 0x400
	v_mfma_f32_32x32x16_bf16 v[64:79], a[240:243], a[176:179], v[64:79]
	ds_read_b64_tr_b16 v[50:51], v215 offset:0x2e00
	ds_read_b64_tr_b16 v[44:45], v215 offset:0x3000
	v_cvt_pk_bf16_f32 v55, v241, v242
	v_add_f32_e32 v32, v32, v241
	v_add_f32_e32 v33, v33, v242
	s_mov_b32 s37, s21
	v_mfma_f32_32x32x16_bf16 v[112:127], a[212:215], a[148:151], v[112:127]
	ds_read_b64_tr_b16 v[46:47], v215 offset:0x3800
	v_add_f32_e32 v32, v32, v227
	v_add_f32_e32 v33, v33, v228
	s_add_i32 s34, s57, 0x800
	s_mov_b32 s38, s34
	v_mfma_f32_32x32x16_bf16 v[96:111], a[212:215], a[180:183], v[96:111]
	ds_read_b64_tr_b16 v[40:41], v215 offset:0x3200
	v_add_f32_e32 v32, v32, v229
	v_add_f32_e32 v33, v33, v230
	s_mov_b32 s39, s22
	v_mfma_f32_32x32x16_bf16 v[80:95], a[244:247], a[148:151], v[80:95]
	ds_read_b64_tr_b16 v[42:43], v215 offset:0x3a00
	v_add_f32_e32 v32, v32, v231
	v_add_f32_e32 v33, v33, v232
	s_add_i32 s40, s57, 0xc00
	v_mfma_f32_32x32x16_bf16 v[64:79], a[244:247], a[180:183], v[64:79]
	ds_read_b64_tr_b16 v[36:37], v215 offset:0x3400
	ds_read_b64_tr_b16 v[38:39], v215 offset:0x3c00
	v_add_f32_e32 v156, v32, v233
	v_add_f32_e32 v157, v33, v234
	s_mov_b32 s41, s23
	v_mfma_f32_32x32x16_bf16 v[112:127], a[216:219], a[152:155], v[112:127]
	ds_read_b64_tr_b16 v[32:33], v215 offset:0x3600
	v_cvt_pk_bf16_f32 v140, v141, v142
	v_add_f32_e32 v158, v237, v141
	v_add_f32_e32 v142, v238, v142
	s_mov_b32 s42, s58
	v_mfma_f32_32x32x16_bf16 v[96:111], a[216:219], a[184:187], v[96:111]
	ds_read_b64_tr_b16 v[34:35], v215 offset:0x3e00
	v_cvt_pk_bf16_f32 v141, v143, v243
	v_add_f32_e32 v143, v158, v143
	v_add_f32_e32 v158, v142, v243
	v_mfma_f32_32x32x16_bf16 v[80:95], a[248:251], a[152:155], v[80:95]
	s_mov_b32 s43, s24
	v_cvt_pk_bf16_f32 v142, v244, v245
	v_add_f32_e32 v159, v143, v244
	v_add_f32_e32 v158, v158, v245
	v_mfma_f32_32x32x16_bf16 v[64:79], a[248:251], a[184:187], v[64:79]
	s_add_i32 s44, s58, 0x80
	v_cvt_pk_bf16_f32 v143, v246, v247
	v_add_f32_e32 v159, v159, v246
	v_add_f32_e32 v158, v158, v247
	v_mfma_f32_32x32x16_bf16 v[112:127], a[220:223], a[156:159], v[112:127]
	s_mov_b32 s45, s25
	v_add_f32_e32 v159, v159, v148
	v_add_f32_e32 v158, v158, v149
	v_mfma_f32_32x32x16_bf16 v[96:111], a[220:223], a[188:191], v[96:111]
	s_add_i32 s46, s58, 0x800
	v_add_f32_e32 v159, v159, v150
	v_add_f32_e32 v158, v158, v151
	v_mfma_f32_32x32x16_bf16 v[80:95], a[252:255], a[156:159], v[80:95]
	s_mov_b32 s47, s26
	v_add_f32_e32 v159, v159, v152
	v_add_f32_e32 v158, v158, v153
	v_mfma_f32_32x32x16_bf16 v[64:79], a[252:255], a[188:191], v[64:79]
	s_add_i32 s48, s58, 0x880
	v_add_f32_e32 v159, v159, v154
	v_add_f32_e32 v158, v158, v155
	v_add_f32_e32 v156, v156, v157
	s_waitcnt vmcnt(0) lgkmcnt(0)
	s_barrier
	s_mov_b32 m0, s0
	v_mfma_f32_32x32x16_bf16 a[0:15], v[172:175], v[164:167], a[0:15]
	v_mov_b32_e32 v157, v156
	buffer_load_dwordx4 v222, s[12:15], s1 offen lds
	s_mov_b32 m0, s35
	v_mfma_f32_32x32x16_bf16 a[16:31], v[172:175], v[192:195], a[16:31]
	v_permlane32_swap_b32_e32 v156, v157
	v_add_f32_e32 v156, v156, v157
	buffer_load_dwordx4 v223, s[12:15], s36 offen lds
	ds_read_b128 a[192:195], v217 offset:0
	s_mov_b32 m0, s37
	v_mfma_f32_32x32x16_bf16 a[32:47], v[184:187], v[164:167], a[32:47]
	v_add_f32_e32 v225, v225, v156
	v_add_f32_e32 v156, v159, v158
	v_mov_b32_e32 v157, v156
	buffer_load_dwordx4 v222, s[12:15], s38 offen lds
	ds_read_b128 a[196:199], v199 offset:0
	s_mov_b32 m0, s39
	v_mfma_f32_32x32x16_bf16 a[48:63], v[184:187], v[192:195], a[48:63]
	v_permlane32_swap_b32_e32 v156, v157
	v_add_f32_e32 v156, v156, v157
	buffer_load_dwordx4 v223, s[12:15], s40 offen lds
	ds_read_b128 a[200:203], v198 offset:0
	s_mov_b32 m0, s41
	v_mfma_f32_32x32x16_bf16 a[64:79], v[180:183], v[164:167], a[64:79]
	v_add_f32_e32 v226, v226, v156
	buffer_load_dwordx4 v196, s[4:7], s42 offen lds
	ds_read_b128 a[204:207], v197 offset:0
	s_mov_b32 m0, s43
	v_mfma_f32_32x32x16_bf16 a[80:95], v[180:183], v[192:195], a[80:95]
	buffer_load_dwordx4 v196, s[4:7], s44 offen lds
	ds_read_b128 a[208:211], v217 offset:128
	s_mov_b32 m0, s45
	v_mfma_f32_32x32x16_bf16 a[96:111], v[188:191], v[164:167], a[96:111]
	buffer_load_dwordx4 v196, s[4:7], s46 offen lds
	ds_read_b128 a[212:215], v199 offset:128
	s_mov_b32 m0, s47
	v_mfma_f32_32x32x16_bf16 a[112:127], v[188:191], v[192:195], a[112:127]
	buffer_load_dwordx4 v196, s[4:7], s48 offen lds
	ds_read_b128 a[216:219], v198 offset:128
	s_nop 0
	v_mfma_f32_32x32x16_bf16 a[0:15], v[176:179], v[128:131], a[0:15]
	ds_read_b128 a[220:223], v197 offset:128
	s_cmp_gt_u32 s27, 12
	s_cbranch_scc1 .Lka_done
	s_cmp_gt_u32 s27, 4
	s_cbranch_scc1 .Lka_single
	v_cvt_pk_bf16_f32 v248, v248, v249
	v_cvt_pk_bf16_f32 v249, v250, v251
	v_cvt_pk_bf16_f32 v250, v252, v253
	v_cvt_pk_bf16_f32 v251, v254, v255
	v_lshrrev_b32_e32 v252, 1, v208
	buffer_store_dwordx4 v[248:251], v252, s[12:15], s56 offen sc1
	v_mbcnt_lo_u32_b32 v253, -1, 0
	v_mbcnt_hi_u32_b32 v253, -1, v253
	v_lshlrev_b32_e32 v253, 4, v253
	v_add_u32_e32 v253, s84, v253
	ds_read_b128 v[248:251], v253
	ds_read_b128 v[252:255], v253 offset:1024
	s_cmp_eq_u32 s27, 2
	s_cbranch_scc0 .Lka_nopub
	s_cmp_eq_u32 s50, 0
	s_cbranch_scc0 .Lf1_pub_done
	v_mov_b32_e32 v210, s70
	s_mov_b64 exec, 1
	global_store_dword v209, v210, s[72:73] offset:3072 sc1
	s_mov_b64 exec, -1

.LBB0_19:
	s_waitcnt lgkmcnt(0)
	v_mfma_f32_32x32x16_bf16 v[112:127], a[192:195], a[128:131], v[0:15]
	v_exp_f32_e32 v80, v80
	v_exp_f32_e32 v81, v81
	ds_read_b64_tr_b16 v[180:181], v212 offset:0
	v_cvt_pk_bf16_f32 v168, v128, v129
	v_exp_f32_e32 v82, v82
	v_exp_f32_e32 v83, v83
	v_mfma_f32_32x32x16_bf16 v[96:111], a[192:195], a[160:163], v[16:31]
	ds_read_b64_tr_b16 v[182:183], v212 offset:0x800
	v_cvt_pk_bf16_f32 v169, v130, v131
	v_mfma_f32_32x32x16_bf16 v[48:63], a[224:227], a[128:131], v[0:15]
	ds_read_b64_tr_b16 v[184:185], v212 offset:0x200
	v_exp_f32_e32 v239, v84
	v_exp_f32_e32 v240, v85
	v_cvt_pk_bf16_f32 v170, v132, v133
	v_mfma_f32_32x32x16_bf16 v[32:47], a[224:227], a[160:163], v[16:31]
	ds_read_b64_tr_b16 v[186:187], v212 offset:0xa00
	ds_read_b64_tr_b16 v[176:177], v212 offset:0x400
	v_exp_f32_e32 v241, v86
	v_exp_f32_e32 v242, v87
	v_cvt_pk_bf16_f32 v171, v134, v135
	v_exp_f32_e32 v227, v88
	v_exp_f32_e32 v228, v89
	v_mfma_f32_32x32x16_bf16 v[112:127], a[196:199], a[132:135], v[112:127]
	ds_read_b64_tr_b16 v[178:179], v212 offset:0xc00
	v_cvt_pk_bf16_f32 v128, v136, v137
	v_exp_f32_e32 v229, v90
	v_exp_f32_e32 v230, v91
	v_mfma_f32_32x32x16_bf16 v[96:111], a[196:199], a[164:167], v[96:111]
	ds_read_b64_tr_b16 v[188:189], v212 offset:0x600
	v_cvt_pk_bf16_f32 v129, v138, v139
	v_exp_f32_e32 v231, v92
	v_exp_f32_e32 v232, v93
	v_mfma_f32_32x32x16_bf16 v[48:63], a[228:231], a[132:135], v[48:63]
	ds_read_b64_tr_b16 v[190:191], v212 offset:0xe00
	v_cvt_pk_bf16_f32 v130, v140, v141
	v_mfma_f32_32x32x16_bf16 v[32:47], a[228:231], a[164:167], v[32:47]
	ds_read_b64_tr_b16 v[172:173], v212 offset:0x1000
	v_exp_f32_e32 v233, v94
	v_exp_f32_e32 v234, v95
	ds_read_b64_tr_b16 v[174:175], v212 offset:0x1800
	v_cvt_pk_bf16_f32 v131, v142, v143
	v_exp_f32_e32 v141, v64
	v_exp_f32_e32 v142, v65
	v_mfma_f32_32x32x16_bf16 v[112:127], a[200:203], a[136:139], v[112:127]
	ds_read_b64_tr_b16 v[164:165], v212 offset:0x1200
	v_cvt_pk_bf16_f32 v192, v144, v145
	v_exp_f32_e32 v143, v66
	v_mfma_f32_32x32x16_bf16 v[96:111], a[200:203], a[168:171], v[96:111]
	ds_read_b64_tr_b16 v[166:167], v212 offset:0x1a00
	v_exp_f32_e32 v243, v67
	v_cvt_pk_bf16_f32 v193, v146, v147
	v_mfma_f32_32x32x16_bf16 v[48:63], a[232:235], a[136:139], v[48:63]
	ds_read_b64_tr_b16 v[160:161], v212 offset:0x1400
	v_exp_f32_e32 v244, v68
	v_exp_f32_e32 v245, v69
	v_cvt_pk_bf16_f32 v194, v148, v149
	v_mfma_f32_32x32x16_bf16 v[32:47], a[232:235], a[168:171], v[32:47]
	ds_read_b64_tr_b16 v[162:163], v212 offset:0x1c00
	ds_read_b64_tr_b16 v[136:137], v212 offset:0x1600
	v_exp_f32_e32 v246, v70
	v_exp_f32_e32 v247, v71
	v_cvt_pk_bf16_f32 v195, v150, v151
	v_exp_f32_e32 v148, v72
	v_exp_f32_e32 v149, v73
	v_mfma_f32_32x32x16_bf16 v[112:127], a[204:207], a[140:143], v[112:127]
	ds_read_b64_tr_b16 v[138:139], v212 offset:0x1e00
	v_cvt_pk_bf16_f32 v144, v152, v153
	v_exp_f32_e32 v150, v74
	v_exp_f32_e32 v151, v75
	v_mfma_f32_32x32x16_bf16 v[96:111], a[204:207], a[172:175], v[96:111]
	ds_read_b64_tr_b16 v[132:133], v212 offset:0x2000
	v_cvt_pk_bf16_f32 v145, v154, v155
	v_exp_f32_e32 v152, v76
	v_exp_f32_e32 v153, v77
	v_mfma_f32_32x32x16_bf16 v[48:63], a[236:239], a[140:143], v[48:63]
	ds_read_b64_tr_b16 v[134:135], v212 offset:0x2800
	v_cvt_pk_bf16_f32 v146, v156, v157
	v_mfma_f32_32x32x16_bf16 v[32:47], a[236:239], a[172:175], v[32:47]
	ds_read_b64_tr_b16 v[92:93], v212 offset:0x2200
	v_exp_f32_e32 v154, v78
	v_exp_f32_e32 v155, v79
	ds_read_b64_tr_b16 v[94:95], v212 offset:0x2a00
	v_cvt_pk_bf16_f32 v147, v158, v159
	s_mov_b32 s0, s3
	v_mfma_f32_32x32x16_bf16 v[112:127], a[208:211], a[144:147], v[112:127]
	ds_read_b64_tr_b16 v[88:89], v212 offset:0x2400
	v_cvt_pk_bf16_f32 v84, v80, v81
	v_add_f32_e32 v64, v236, v80
	v_add_f32_e32 v65, v235, v81
	s_add_i32 s58, s57, s60
	s_and_b32 s58, s58, 0x7ffff
	s_mov_b32 s1, s58
	v_mfma_f32_32x32x16_bf16 v[96:111], a[208:211], a[176:179], v[96:111]
	ds_read_b64_tr_b16 v[90:91], v212 offset:0x2c00
	v_cvt_pk_bf16_f32 v85, v82, v83
	v_add_f32_e32 v64, v64, v82
	v_add_f32_e32 v65, v65, v83
	s_mov_b32 s35, s10
	v_mfma_f32_32x32x16_bf16 v[48:63], a[240:243], a[144:147], v[48:63]
	ds_read_b64_tr_b16 v[80:81], v212 offset:0x2600
	v_cvt_pk_bf16_f32 v86, v239, v240
	v_add_f32_e32 v64, v64, v239
	v_add_f32_e32 v65, v65, v240
	s_add_i32 s36, s58, 0x400
	v_mfma_f32_32x32x16_bf16 v[32:47], a[240:243], a[176:179], v[32:47]
	ds_read_b64_tr_b16 v[82:83], v212 offset:0x2e00
	ds_read_b64_tr_b16 v[76:77], v212 offset:0x3000
	v_cvt_pk_bf16_f32 v87, v241, v242
	v_add_f32_e32 v64, v64, v241
	v_add_f32_e32 v65, v65, v242
	s_mov_b32 s37, s11
	v_mfma_f32_32x32x16_bf16 v[112:127], a[212:215], a[148:151], v[112:127]
	ds_read_b64_tr_b16 v[78:79], v212 offset:0x3800
	v_add_f32_e32 v64, v64, v227
	v_add_f32_e32 v65, v65, v228
	s_add_i32 s38, s58, 0x800
	v_mfma_f32_32x32x16_bf16 v[96:111], a[212:215], a[180:183], v[96:111]
	ds_read_b64_tr_b16 v[72:73], v212 offset:0x3200
	v_add_f32_e32 v64, v64, v229
	v_add_f32_e32 v65, v65, v230
	s_mov_b32 s39, s16
	v_mfma_f32_32x32x16_bf16 v[48:63], a[244:247], a[148:151], v[48:63]
	ds_read_b64_tr_b16 v[74:75], v212 offset:0x3a00
	v_add_f32_e32 v64, v64, v231
	v_add_f32_e32 v65, v65, v232
	s_add_i32 s40, s58, 0xc00
	v_mfma_f32_32x32x16_bf16 v[32:47], a[244:247], a[180:183], v[32:47]
	ds_read_b64_tr_b16 v[68:69], v212 offset:0x3400
	ds_read_b64_tr_b16 v[70:71], v212 offset:0x3c00
	v_add_f32_e32 v156, v64, v233
	v_add_f32_e32 v157, v65, v234
	s_mov_b32 s41, s2
	v_mfma_f32_32x32x16_bf16 v[112:127], a[216:219], a[152:155], v[112:127]
	ds_read_b64_tr_b16 v[64:65], v212 offset:0x3600
	v_cvt_pk_bf16_f32 v140, v141, v142
	v_add_f32_e32 v158, v237, v141
	v_add_f32_e32 v142, v238, v142
	v_mfma_f32_32x32x16_bf16 v[96:111], a[216:219], a[184:187], v[96:111]
	ds_read_b64_tr_b16 v[66:67], v212 offset:0x3e00
	v_cvt_pk_bf16_f32 v141, v143, v243
	v_add_f32_e32 v143, v158, v143
	v_add_f32_e32 v158, v142, v243
	v_mfma_f32_32x32x16_bf16 v[48:63], a[248:251], a[152:155], v[48:63]
	s_mov_b32 s42, s17
	v_cvt_pk_bf16_f32 v142, v244, v245
	v_add_f32_e32 v159, v143, v244
	v_add_f32_e32 v158, v158, v245
	v_mfma_f32_32x32x16_bf16 v[32:47], a[248:251], a[184:187], v[32:47]
	s_add_i32 s43, s57, 0x80
	v_cvt_pk_bf16_f32 v143, v246, v247
	v_add_f32_e32 v159, v159, v246
	v_add_f32_e32 v158, v158, v247
	v_mfma_f32_32x32x16_bf16 v[112:127], a[220:223], a[156:159], v[112:127]
	s_mov_b32 s44, s18
	v_add_f32_e32 v159, v159, v148
	v_add_f32_e32 v158, v158, v149
	v_mfma_f32_32x32x16_bf16 v[96:111], a[220:223], a[188:191], v[96:111]
	v_add_f32_e32 v159, v159, v150
	v_add_f32_e32 v158, v158, v151
	v_mfma_f32_32x32x16_bf16 v[48:63], a[252:255], a[156:159], v[48:63]
	s_mov_b32 s45, s19
	v_add_f32_e32 v159, v159, v152
	v_add_f32_e32 v158, v158, v153
	v_mfma_f32_32x32x16_bf16 v[32:47], a[252:255], a[188:191], v[32:47]
	s_add_i32 s46, s57, 0x880
	v_add_f32_e32 v159, v159, v154
	v_add_f32_e32 v158, v158, v155
	v_add_f32_e32 v156, v156, v157
	s_waitcnt vmcnt(0) lgkmcnt(0)
	s_barrier
	s_mov_b32 m0, s0
	v_mfma_f32_32x32x16_bf16 a[0:15], v[180:183], v[168:171], a[0:15]
	v_mov_b32_e32 v157, v156
	buffer_load_dwordx4 v222, s[12:15], s1 offen lds
	s_mov_b32 m0, s35
	v_mfma_f32_32x32x16_bf16 a[16:31], v[180:183], v[192:195], a[16:31]
	v_permlane32_swap_b32_e32 v156, v157
	v_add_f32_e32 v156, v156, v157
	buffer_load_dwordx4 v223, s[12:15], s36 offen lds
	ds_read_b128 a[192:195], v218 offset:0
	s_mov_b32 m0, s37
	v_mfma_f32_32x32x16_bf16 a[32:47], v[184:187], v[168:171], a[32:47]
	v_add_f32_e32 v225, v225, v156
	v_add_f32_e32 v156, v159, v158
	v_mov_b32_e32 v157, v156
	buffer_load_dwordx4 v222, s[12:15], s38 offen lds
	ds_read_b128 a[196:199], v219 offset:0
	s_mov_b32 m0, s39
	v_mfma_f32_32x32x16_bf16 a[48:63], v[184:187], v[192:195], a[48:63]
	v_permlane32_swap_b32_e32 v156, v157
	v_add_f32_e32 v156, v156, v157
	buffer_load_dwordx4 v223, s[12:15], s40 offen lds
	ds_read_b128 a[200:203], v220 offset:0
	s_mov_b32 m0, s41
	v_mfma_f32_32x32x16_bf16 a[64:79], v[176:179], v[168:171], a[64:79]
	v_add_f32_e32 v226, v226, v156
	buffer_load_dwordx4 v196, s[4:7], s33 offen lds
	ds_read_b128 a[204:207], v221 offset:0
	s_mov_b32 m0, s42
	v_mfma_f32_32x32x16_bf16 a[80:95], v[176:179], v[192:195], a[80:95]
	buffer_load_dwordx4 v196, s[4:7], s43 offen lds
	ds_read_b128 a[208:211], v218 offset:128
	s_mov_b32 m0, s44
	v_mfma_f32_32x32x16_bf16 a[96:111], v[188:191], v[168:171], a[96:111]
	buffer_load_dwordx4 v196, s[4:7], s34 offen lds
	ds_read_b128 a[212:215], v219 offset:128
	s_mov_b32 m0, s45
	v_mfma_f32_32x32x16_bf16 a[112:127], v[188:191], v[192:195], a[112:127]
	buffer_load_dwordx4 v196, s[4:7], s46 offen lds
	ds_read_b128 a[216:219], v220 offset:128
	s_nop 0
	v_mfma_f32_32x32x16_bf16 a[0:15], v[172:175], v[128:131], a[0:15]
	ds_read_b128 a[220:223], v221 offset:128
	s_cmp_gt_u32 s27, 12
	s_cbranch_scc1 .Lkc_done
	s_cmp_gt_u32 s27, 4
	s_cbranch_scc1 .Lkc_single
	v_cvt_pk_bf16_f32 v248, v248, v249
	v_cvt_pk_bf16_f32 v249, v250, v251
	v_cvt_pk_bf16_f32 v250, v252, v253
	v_cvt_pk_bf16_f32 v251, v254, v255
	v_lshrrev_b32_e32 v252, 1, v208
	buffer_store_dwordx4 v[248:251], v252, s[12:15], s56 offen sc1
	v_mbcnt_lo_u32_b32 v253, -1, 0
	v_mbcnt_hi_u32_b32 v253, -1, v253
	v_lshlrev_b32_e32 v253, 4, v253
	v_add_u32_e32 v253, s84, v253
	ds_read_b128 v[248:251], v253
	ds_read_b128 v[252:255], v253 offset:1024
	s_branch .Lkc_done

.LBB0_36:
	s_lshl_b32 s53, s50, 6
	s_add_i32 s53, s53, s52
	v_mov_b32_e32 v200, s53
	s_lshl_b32 s53, s50, 14
	s_add_i32 s53, s53, 0x10000
	v_mov_b32_e32 v201, s53
	v_mbcnt_lo_u32_b32 v204, -1, 0
	v_mbcnt_hi_u32_b32 v204, -1, v204
	v_lshrrev_b32_e32 v202, 4, v204
	v_add_u32_e32 v203, 4, v202
	v_add_u32_e32 v205, 8, v202
	v_add_u32_e32 v206, 12, v202
	v_add_u32_e32 v207, 16, v202
	v_add_u32_e32 v208, 20, v202
	v_add_u32_e32 v209, 24, v202
	v_add_u32_e32 v210, 28, v202
	v_mfma_f32_32x32x16_bf16 v[112:127], a[192:195], a[128:131], v[0:15]
	v_exp_f32_e32 v48, v48
	v_exp_f32_e32 v49, v49
	ds_read_b64_tr_b16 v[180:181], v215 offset:0
	v_cvt_pk_bf16_f32 v164, v128, v129
	v_exp_f32_e32 v50, v50
	v_exp_f32_e32 v51, v51
	v_mfma_f32_32x32x16_bf16 v[96:111], a[192:195], a[160:163], v[16:31]
	ds_read_b64_tr_b16 v[182:183], v215 offset:0x800
	v_cvt_pk_bf16_f32 v165, v130, v131
	v_mfma_f32_32x32x16_bf16 v[80:95], a[224:227], a[128:131], v[0:15]
	v_exp_f32_e32 v218, v52
	v_exp_f32_e32 v219, v53
	ds_read_b64_tr_b16 v[188:189], v215 offset:0x200
	v_cvt_pk_bf16_f32 v166, v132, v133
	v_mfma_f32_32x32x16_bf16 v[64:79], a[224:227], a[160:163], v[16:31]
	ds_read_b64_tr_b16 v[190:191], v215 offset:0xa00
	ds_read_b64_tr_b16 v[176:177], v215 offset:0x400
	v_exp_f32_e32 v230, v54
	v_exp_f32_e32 v231, v55
	v_cvt_pk_bf16_f32 v167, v134, v135
	v_exp_f32_e32 v220, v56
	v_exp_f32_e32 v221, v57
	v_mfma_f32_32x32x16_bf16 v[112:127], a[196:199], a[132:135], v[112:127]
	ds_read_b64_tr_b16 v[178:179], v215 offset:0xc00
	v_cvt_pk_bf16_f32 v128, v136, v137
	v_exp_f32_e32 v222, v58
	v_exp_f32_e32 v223, v59
	v_mfma_f32_32x32x16_bf16 v[96:111], a[196:199], a[164:167], v[96:111]
	ds_read_b64_tr_b16 v[184:185], v215 offset:0x600
	v_cvt_pk_bf16_f32 v129, v138, v139
	v_exp_f32_e32 v224, v60
	v_exp_f32_e32 v227, v61
	v_mfma_f32_32x32x16_bf16 v[80:95], a[228:231], a[132:135], v[80:95]
	ds_read_b64_tr_b16 v[186:187], v215 offset:0xe00
	v_cvt_pk_bf16_f32 v130, v140, v141
	v_mfma_f32_32x32x16_bf16 v[64:79], a[228:231], a[164:167], v[64:79]
	ds_read_b64_tr_b16 v[172:173], v215 offset:0x1000
	v_exp_f32_e32 v228, v62
	v_exp_f32_e32 v229, v63
	ds_read_b64_tr_b16 v[174:175], v215 offset:0x1800
	v_cvt_pk_bf16_f32 v131, v142, v143
	v_exp_f32_e32 v141, v32
	v_exp_f32_e32 v142, v33
	v_mfma_f32_32x32x16_bf16 v[112:127], a[200:203], a[136:139], v[112:127]
	ds_read_b64_tr_b16 v[168:169], v215 offset:0x1200
	v_cvt_pk_bf16_f32 v192, v144, v145
	v_exp_f32_e32 v143, v34
	v_mfma_f32_32x32x16_bf16 v[96:111], a[200:203], a[168:171], v[96:111]
	ds_read_b64_tr_b16 v[170:171], v215 offset:0x1a00
	v_exp_f32_e32 v232, v35
	v_cvt_pk_bf16_f32 v193, v146, v147
	v_mfma_f32_32x32x16_bf16 v[80:95], a[232:235], a[136:139], v[80:95]
	ds_read_b64_tr_b16 v[160:161], v215 offset:0x1400
	v_exp_f32_e32 v233, v36
	v_exp_f32_e32 v234, v37
	v_cvt_pk_bf16_f32 v194, v148, v149
	v_mfma_f32_32x32x16_bf16 v[64:79], a[232:235], a[168:171], v[64:79]
	ds_read_b64_tr_b16 v[162:163], v215 offset:0x1c00
	ds_read_b64_tr_b16 v[136:137], v215 offset:0x1600
	v_exp_f32_e32 v239, v38
	v_exp_f32_e32 v240, v39
	v_cvt_pk_bf16_f32 v195, v150, v151
	v_exp_f32_e32 v148, v40
	v_exp_f32_e32 v149, v41
	v_mfma_f32_32x32x16_bf16 v[112:127], a[204:207], a[140:143], v[112:127]
	ds_read_b64_tr_b16 v[138:139], v215 offset:0x1e00
	v_cvt_pk_bf16_f32 v144, v152, v153
	v_exp_f32_e32 v150, v42
	v_exp_f32_e32 v151, v43
	v_mfma_f32_32x32x16_bf16 v[96:111], a[204:207], a[172:175], v[96:111]
	ds_read_b64_tr_b16 v[132:133], v215 offset:0x2000
	v_cvt_pk_bf16_f32 v145, v154, v155
	v_exp_f32_e32 v152, v44
	v_exp_f32_e32 v153, v45
	v_mfma_f32_32x32x16_bf16 v[80:95], a[236:239], a[140:143], v[80:95]
	ds_read_b64_tr_b16 v[134:135], v215 offset:0x2800
	v_cvt_pk_bf16_f32 v146, v156, v157
	v_mfma_f32_32x32x16_bf16 v[64:79], a[236:239], a[172:175], v[64:79]
	ds_read_b64_tr_b16 v[60:61], v215 offset:0x2200
	v_exp_f32_e32 v154, v46
	v_exp_f32_e32 v155, v47
	ds_read_b64_tr_b16 v[62:63], v215 offset:0x2a00
	v_cvt_pk_bf16_f32 v147, v158, v159
	v_mfma_f32_32x32x16_bf16 v[112:127], a[208:211], a[144:147], v[112:127]
	ds_read_b64_tr_b16 v[56:57], v215 offset:0x2400
	v_cvt_pk_bf16_f32 v52, v48, v49
	v_add_f32_e32 v32, v236, v48
	v_add_f32_e32 v33, v235, v49
	s_add_i32 s12, s28, 0x80000
	s_mov_b32 s0, s12
	v_mfma_f32_32x32x16_bf16 v[96:111], a[208:211], a[176:179], v[96:111]
	ds_read_b64_tr_b16 v[58:59], v215 offset:0x2c00
	v_cvt_pk_bf16_f32 v53, v50, v51
	v_add_f32_e32 v32, v32, v50
	v_add_f32_e32 v33, v33, v51
	v_mfma_f32_32x32x16_bf16 v[80:95], a[240:243], a[144:147], v[80:95]
	ds_read_b64_tr_b16 v[48:49], v215 offset:0x2600
	v_cvt_pk_bf16_f32 v54, v218, v219
	v_add_f32_e32 v32, v32, v218
	v_add_f32_e32 v33, v33, v219
	s_add_i32 s1, s28, 0x80400
	v_mfma_f32_32x32x16_bf16 v[64:79], a[240:243], a[176:179], v[64:79]
	ds_read_b64_tr_b16 v[50:51], v215 offset:0x2e00
	ds_read_b64_tr_b16 v[44:45], v215 offset:0x3000
	v_cvt_pk_bf16_f32 v55, v230, v231
	v_add_f32_e32 v32, v32, v230
	v_add_f32_e32 v33, v33, v231
	v_mfma_f32_32x32x16_bf16 v[112:127], a[212:215], a[148:151], v[112:127]
	ds_read_b64_tr_b16 v[46:47], v215 offset:0x3800
	v_add_f32_e32 v32, v32, v220
	v_add_f32_e32 v33, v33, v221
	s_add_i32 s13, s28, 0x80800
	s_mov_b32 s14, s13
	v_mfma_f32_32x32x16_bf16 v[96:111], a[212:215], a[180:183], v[96:111]
	ds_read_b64_tr_b16 v[40:41], v215 offset:0x3200
	v_add_f32_e32 v32, v32, v222
	v_add_f32_e32 v33, v33, v223
	v_mfma_f32_32x32x16_bf16 v[80:95], a[244:247], a[148:151], v[80:95]
	ds_read_b64_tr_b16 v[42:43], v215 offset:0x3a00
	v_add_f32_e32 v32, v32, v224
	v_add_f32_e32 v33, v33, v227
	s_add_i32 s15, s28, 0x80c00
	v_mfma_f32_32x32x16_bf16 v[64:79], a[244:247], a[180:183], v[64:79]
	ds_read_b64_tr_b16 v[36:37], v215 offset:0x3400
	ds_read_b64_tr_b16 v[38:39], v215 offset:0x3c00
	v_add_f32_e32 v156, v32, v228
	v_add_f32_e32 v157, v33, v229
	v_mfma_f32_32x32x16_bf16 v[112:127], a[216:219], a[152:155], v[112:127]
	ds_read_b64_tr_b16 v[32:33], v215 offset:0x3600
	v_cvt_pk_bf16_f32 v140, v141, v142
	v_add_f32_e32 v158, v237, v141
	v_add_f32_e32 v142, v238, v142
	s_add_i32 s27, s88, 0x0
	v_mfma_f32_32x32x16_bf16 v[96:111], a[216:219], a[184:187], v[96:111]
	ds_read_b64_tr_b16 v[34:35], v215 offset:0x3e00
	v_cvt_pk_bf16_f32 v141, v143, v232
	v_add_f32_e32 v143, v158, v143
	v_add_f32_e32 v158, v142, v232
	v_mfma_f32_32x32x16_bf16 v[80:95], a[248:251], a[152:155], v[80:95]
	v_cvt_pk_bf16_f32 v142, v233, v234
	v_add_f32_e32 v159, v143, v233
	v_add_f32_e32 v158, v158, v234
	v_mfma_f32_32x32x16_bf16 v[64:79], a[248:251], a[184:187], v[64:79]
	s_add_i32 s30, s88, 0x80
	v_cvt_pk_bf16_f32 v143, v239, v240
	v_add_f32_e32 v159, v159, v239
	v_add_f32_e32 v158, v158, v240
	v_mfma_f32_32x32x16_bf16 v[112:127], a[220:223], a[156:159], v[112:127]
	v_add_f32_e32 v159, v159, v148
	v_add_f32_e32 v158, v158, v149
	v_mfma_f32_32x32x16_bf16 v[96:111], a[220:223], a[188:191], v[96:111]
	s_add_i32 s31, s88, 0x800
	v_add_f32_e32 v159, v159, v150
	v_add_f32_e32 v158, v158, v151
	v_mfma_f32_32x32x16_bf16 v[80:95], a[252:255], a[156:159], v[80:95]
	v_add_f32_e32 v159, v159, v152
	v_add_f32_e32 v158, v158, v153
	v_mfma_f32_32x32x16_bf16 v[64:79], a[252:255], a[188:191], v[64:79]
	s_add_i32 s33, s88, 0x880
	v_add_f32_e32 v159, v159, v154
	v_add_f32_e32 v158, v158, v155
	v_add_f32_e32 v156, v156, v157
	s_waitcnt vmcnt(0) lgkmcnt(0)
	s_barrier
	v_mfma_f32_32x32x16_bf16 a[0:15], v[180:183], v[164:167], a[0:15]
	v_mov_b32_e32 v157, v156
	v_mfma_f32_32x32x16_bf16 a[16:31], v[180:183], v[192:195], a[16:31]
	s_nop 1
	v_permlane32_swap_b32_e32 v156, v157
	v_add_f32_e32 v156, v156, v157
	ds_read_b128 a[192:195], v217 offset:0
	v_mfma_f32_32x32x16_bf16 a[32:47], v[188:191], v[164:167], a[32:47]
	v_add_f32_e32 v219, v225, v156
	v_add_f32_e32 v156, v159, v158
	v_mov_b32_e32 v157, v156
	ds_read_b128 a[196:199], v199 offset:0
	v_mfma_f32_32x32x16_bf16 a[48:63], v[188:191], v[192:195], a[48:63]
	v_permlane32_swap_b32_e32 v156, v157
	v_add_f32_e32 v156, v156, v157
	ds_read_b128 a[200:203], v198 offset:0
	s_mov_b32 m0, s23
	v_mfma_f32_32x32x16_bf16 a[64:79], v[176:179], v[164:167], a[64:79]
	v_add_f32_e32 v218, v226, v156
	buffer_load_dwordx4 v196, s[4:7], s27 offen lds
	ds_read_b128 a[204:207], v197 offset:0
	s_mov_b32 m0, s24
	v_mfma_f32_32x32x16_bf16 a[80:95], v[176:179], v[192:195], a[80:95]
	buffer_load_dwordx4 v196, s[4:7], s30 offen lds
	ds_read_b128 a[208:211], v217 offset:128
	s_mov_b32 m0, s25
	v_mfma_f32_32x32x16_bf16 a[96:111], v[184:187], v[164:167], a[96:111]
	buffer_load_dwordx4 v196, s[4:7], s31 offen lds
	ds_read_b128 a[212:215], v199 offset:128
	s_mov_b32 m0, s26
	v_mfma_f32_32x32x16_bf16 a[112:127], v[184:187], v[192:195], a[112:127]
	buffer_load_dwordx4 v196, s[4:7], s33 offen lds
	ds_read_b128 a[216:219], v198 offset:128
	v_mfma_f32_32x32x16_bf16 a[0:15], v[172:175], v[128:131], a[0:15]
	ds_read_b128 a[220:223], v197 offset:128
	v_max3_f32 v156, v112, v113, v80
	v_max3_f32 v157, v114, v115, v81
	v_max3_f32 v156, v156, v82, v83
	v_mfma_f32_32x32x16_bf16 a[16:31], v[172:175], v[144:147], a[16:31]
	ds_read_b128 a[224:227], v217 offset:8192
	v_max3_f32 v156, v156, v116, v117
	v_max3_f32 v157, v157, v118, v119
	v_max3_f32 v156, v156, v84, v85
	v_max3_f32 v157, v157, v86, v87
	v_mfma_f32_32x32x16_bf16 a[32:47], v[168:171], v[128:131], a[32:47]
	ds_read_b128 a[228:231], v199 offset:8192
	v_max3_f32 v156, v156, v120, v121
	v_max3_f32 v157, v157, v122, v123
	v_max3_f32 v156, v156, v88, v89
	v_max3_f32 v157, v157, v90, v91
	v_mfma_f32_32x32x16_bf16 a[48:63], v[168:171], v[144:147], a[48:63]
	ds_read_b128 a[232:235], v198 offset:8192
	v_max3_f32 v156, v156, v124, v125
	v_max3_f32 v157, v157, v126, v127
	v_max3_f32 v156, v156, v92, v93
	v_max3_f32 v157, v157, v94, v95
	v_mfma_f32_32x32x16_bf16 a[64:79], v[160:163], v[128:131], a[64:79]
	ds_read_b128 a[236:239], v197 offset:8192
	v_max3_f32 v158, v96, v97, v64
	v_max3_f32 v159, v98, v99, v65
	v_max3_f32 v158, v158, v66, v67
	v_mfma_f32_32x32x16_bf16 a[80:95], v[160:163], v[144:147], a[80:95]
	ds_read_b128 a[240:243], v217 offset:8320
	v_max3_f32 v158, v158, v100, v101
	v_max3_f32 v159, v159, v102, v103
	v_max3_f32 v158, v158, v68, v69
	v_max3_f32 v159, v159, v70, v71
	v_mfma_f32_32x32x16_bf16 a[96:111], v[136:139], v[128:131], a[96:111]
	ds_read_b128 a[244:247], v199 offset:8320
	v_max3_f32 v128, v158, v104, v105
	v_max3_f32 v129, v159, v106, v107
	v_max3_f32 v128, v128, v72, v73
	v_max3_f32 v129, v129, v74, v75
	v_mfma_f32_32x32x16_bf16 a[112:127], v[136:139], v[144:147], a[112:127]
	ds_read_b128 a[248:251], v198 offset:8320
	v_max3_f32 v128, v128, v108, v109
	v_max3_f32 v129, v129, v110, v111
	v_max3_f32 v128, v128, v76, v77
	v_max3_f32 v130, v129, v78, v79
	v_mfma_f32_32x32x16_bf16 a[0:15], v[132:135], v[52:55], a[0:15]
	ds_read_b128 a[252:255], v197 offset:8320
	v_max_f32_e32 v129, v156, v157
	v_mov_b32_e32 v131, v129
	s_nop 1
	v_permlane32_swap_b32_e32 v129, v131
	v_max_f32_e32 v129, v129, v131
	v_mfma_f32_32x32x16_bf16 a[16:31], v[132:135], v[140:143], a[16:31]
	v_max_f32_e32 v128, v128, v130
	v_mov_b32_e32 v130, v128
	s_nop 1
	v_permlane32_swap_b32_e32 v128, v130
	v_max_f32_e32 v128, v128, v130
	v_max_f32_e32 v130, v129, v129
	v_max_f32_e32 v131, v128, v128
	v_max_f32_e32 v130, v130, v131
	s_mov_b32 s0, 0x41000000
	v_mfma_f32_32x32x16_bf16 a[32:47], v[60:63], v[52:55], a[32:47]
	v_cmp_lt_f32_e32 vcc, s0, v130
	s_cmp_lg_u64 vcc, 0
	s_cselect_b64 s[0:1], -1, 0
	s_cbranch_vccnz .LBB0_43
